# combo12a + nt on the read-once residual loads of the P4 (x, f32) and P10 (x1, bf16) epilogues
# baseline (speedup 1.0000x reference)
.LBB0_565:
	s_andn2_b64 vcc, exec, s[4:5]
	s_mov_b64 s[4:5], -1
	s_ashr_i32 s21, s28, 4
	s_mul_hi_i32 s23, s21, 0x18000
	s_mul_i32 s21, s21, 0x18000
	s_add_u32 s30, s45, s21
	s_addc_u32 s31, s46, s23
	v_lshl_or_b32 v224, s54, 8, v197
	v_mov_b32_e32 v225, 0
	v_lshl_add_u64 v[226:227], v[224:225], 2, s[30:31]
	global_load_dwordx4 v[200:203], v[226:227], off
	global_load_dwordx4 v[204:207], v[226:227], off offset:64
	global_load_dwordx4 v[208:211], v[226:227], off offset:512
	global_load_dwordx4 v[212:215], v[226:227], off offset:576
	v_lshl_add_u32 v228, s28, 8, v180
	v_mov_b32_e32 v229, 0
	v_lshlrev_b64 v[216:217], 14, v[228:229]
	v_lshl_add_u64 v[216:217], v[216:217], 0, s[8:9]
	v_lshl_add_u64 v[216:217], v[224:225], 2, v[216:217]
	v_lshlrev_b64 v[218:219], 13, v[228:229]
	v_lshl_add_u64 v[218:219], v[218:219], 0, s[12:13]
	v_and_b32_e32 v230, 12, v197
	v_add_u32_e32 v230, v230, v224
	v_mov_b32_e32 v231, 0
	v_lshl_add_u64 v[218:219], v[230:231], 1, v[218:219]
	s_mov_b32 s30, 0x0
	s_mov_b32 s31, 0
	v_lshl_add_u64 v[220:221], v[216:217], 0, s[30:31]
	global_load_dwordx4 v[0:3], v[220:221], off nt
	global_load_dwordx4 v[4:7], v[220:221], off offset:64 nt
	s_mov_b32 s30, 0x0
	s_mov_b32 s31, 0
	v_lshl_add_u64 v[220:221], v[216:217], 0, s[30:31]
	global_load_dwordx4 v[8:11], v[220:221], off offset:512 nt
	global_load_dwordx4 v[12:15], v[220:221], off offset:576 nt
	s_mov_b32 s30, 0x40000
	s_mov_b32 s31, 0
	v_lshl_add_u64 v[220:221], v[216:217], 0, s[30:31]
	global_load_dwordx4 v[16:19], v[220:221], off nt
	global_load_dwordx4 v[20:23], v[220:221], off offset:64 nt
	s_mov_b32 s30, 0x40000
	s_mov_b32 s31, 0
	v_lshl_add_u64 v[220:221], v[216:217], 0, s[30:31]
	global_load_dwordx4 v[24:27], v[220:221], off offset:512 nt
	global_load_dwordx4 v[28:31], v[220:221], off offset:576 nt
	s_mov_b32 s30, 0x80000
	s_mov_b32 s31, 0
	v_lshl_add_u64 v[220:221], v[216:217], 0, s[30:31]
	global_load_dwordx4 v[172:175], v[220:221], off nt
	global_load_dwordx4 v[176:179], v[220:221], off offset:64 nt
	s_waitcnt vmcnt(10)
	v_mul_f32_e32 v200, s18, v200
	v_mul_f32_e32 v201, s18, v201
	v_mul_f32_e32 v202, s18, v202
	v_mul_f32_e32 v203, s18, v203
	v_mul_f32_e32 v204, s18, v204
	v_mul_f32_e32 v205, s18, v205
	v_mul_f32_e32 v206, s18, v206
	v_mul_f32_e32 v207, s18, v207
	v_mul_f32_e32 v208, s18, v208
	v_mul_f32_e32 v209, s18, v209
	v_mul_f32_e32 v210, s18, v210
	v_mul_f32_e32 v211, s18, v211
	v_mul_f32_e32 v212, s18, v212
	v_mul_f32_e32 v213, s18, v213
	v_mul_f32_e32 v214, s18, v214
	v_mul_f32_e32 v215, s18, v215
	s_waitcnt vmcnt(8)
	v_fma_f32 v0, v156, v200, v0
	v_fma_f32 v1, v157, v201, v1
	v_fma_f32 v2, v158, v202, v2
	v_fma_f32 v3, v159, v203, v3
	v_fma_f32 v4, v152, v204, v4
	v_fma_f32 v5, v153, v205, v5
	v_fma_f32 v6, v154, v206, v6
	v_fma_f32 v7, v155, v207, v7
	v_cvt_pk_bf16_f32 v0, v0, v1
	v_cvt_pk_bf16_f32 v1, v2, v3
	v_cvt_pk_bf16_f32 v2, v4, v5
	v_cvt_pk_bf16_f32 v3, v6, v7
	s_mov_b32 s30, 0x0
	s_mov_b32 s31, 0
	v_lshl_add_u64 v[222:223], v[218:219], 0, s[30:31]
	s_nop 1
	v_permlane32_swap_b32_e32 v0, v2
	v_permlane32_swap_b32_e32 v1, v3
	s_nop 1
	v_permlane16_swap_b32_e32 v0, v2
	v_permlane16_swap_b32_e32 v1, v3
	global_store_dwordx4 v[222:223], v[0:3], off
	s_mov_b32 s30, 0x80000
	s_mov_b32 s31, 0
	v_lshl_add_u64 v[220:221], v[216:217], 0, s[30:31]
	global_load_dwordx4 v[0:3], v[220:221], off offset:512 nt
	global_load_dwordx4 v[4:7], v[220:221], off offset:576 nt
	s_waitcnt vmcnt(9)
	v_fma_f32 v8, v140, v208, v8
	v_fma_f32 v9, v141, v209, v9
	v_fma_f32 v10, v142, v210, v10
	v_fma_f32 v11, v143, v211, v11
	v_fma_f32 v12, v136, v212, v12
	v_fma_f32 v13, v137, v213, v13
	v_fma_f32 v14, v138, v214, v14
	v_fma_f32 v15, v139, v215, v15
	v_cvt_pk_bf16_f32 v8, v8, v9
	v_cvt_pk_bf16_f32 v9, v10, v11
	v_cvt_pk_bf16_f32 v10, v12, v13
	v_cvt_pk_bf16_f32 v11, v14, v15
	s_mov_b32 s30, 0x0
	s_mov_b32 s31, 0
	v_lshl_add_u64 v[222:223], v[218:219], 0, s[30:31]
	s_nop 1
	v_permlane32_swap_b32_e32 v8, v10
	v_permlane32_swap_b32_e32 v9, v11
	s_nop 1
	v_permlane16_swap_b32_e32 v8, v10
	v_permlane16_swap_b32_e32 v9, v11
	global_store_dwordx4 v[222:223], v[8:11], off offset:256
	s_mov_b32 s30, 0xc0000
	s_mov_b32 s31, 0
	v_lshl_add_u64 v[220:221], v[216:217], 0, s[30:31]
	global_load_dwordx4 v[8:11], v[220:221], off nt
	global_load_dwordx4 v[12:15], v[220:221], off offset:64 nt
	s_waitcnt vmcnt(10)
	v_fma_f32 v16, v148, v200, v16
	v_fma_f32 v17, v149, v201, v17
	v_fma_f32 v18, v150, v202, v18
	v_fma_f32 v19, v151, v203, v19
	v_fma_f32 v20, v144, v204, v20
	v_fma_f32 v21, v145, v205, v21
	v_fma_f32 v22, v146, v206, v22
	v_fma_f32 v23, v147, v207, v23
	v_cvt_pk_bf16_f32 v16, v16, v17
	v_cvt_pk_bf16_f32 v17, v18, v19
	v_cvt_pk_bf16_f32 v18, v20, v21
	v_cvt_pk_bf16_f32 v19, v22, v23
	s_mov_b32 s30, 0x20000
	s_mov_b32 s31, 0
	v_lshl_add_u64 v[222:223], v[218:219], 0, s[30:31]
	s_nop 1
	v_permlane32_swap_b32_e32 v16, v18
	v_permlane32_swap_b32_e32 v17, v19
	s_nop 1
	v_permlane16_swap_b32_e32 v16, v18
	v_permlane16_swap_b32_e32 v17, v19
	global_store_dwordx4 v[222:223], v[16:19], off
	s_mov_b32 s30, 0xc0000
	s_mov_b32 s31, 0
	v_lshl_add_u64 v[220:221], v[216:217], 0, s[30:31]
	global_load_dwordx4 v[16:19], v[220:221], off offset:512 nt
	global_load_dwordx4 v[20:23], v[220:221], off offset:576 nt
	s_waitcnt vmcnt(11)
	v_fma_f32 v24, v132, v208, v24
	v_fma_f32 v25, v133, v209, v25
	v_fma_f32 v26, v134, v210, v26
	v_fma_f32 v27, v135, v211, v27
	v_fma_f32 v28, v128, v212, v28
	v_fma_f32 v29, v129, v213, v29
	v_fma_f32 v30, v130, v214, v30
	v_fma_f32 v31, v131, v215, v31
	v_cvt_pk_bf16_f32 v24, v24, v25
	v_cvt_pk_bf16_f32 v25, v26, v27
	v_cvt_pk_bf16_f32 v26, v28, v29
	v_cvt_pk_bf16_f32 v27, v30, v31
	s_mov_b32 s30, 0x20000
	s_mov_b32 s31, 0
	v_lshl_add_u64 v[222:223], v[218:219], 0, s[30:31]
	s_nop 1
	v_permlane32_swap_b32_e32 v24, v26
	v_permlane32_swap_b32_e32 v25, v27
	s_nop 1
	v_permlane16_swap_b32_e32 v24, v26
	v_permlane16_swap_b32_e32 v25, v27
	global_store_dwordx4 v[222:223], v[24:27], off offset:256
	s_mov_b32 s30, 0x200000
	s_mov_b32 s31, 0
	v_lshl_add_u64 v[220:221], v[216:217], 0, s[30:31]
	global_load_dwordx4 v[24:27], v[220:221], off nt
	global_load_dwordx4 v[28:31], v[220:221], off offset:64 nt
	s_waitcnt vmcnt(12)
	v_fma_f32 v172, v124, v200, v172
	v_fma_f32 v173, v125, v201, v173
	v_fma_f32 v174, v126, v202, v174
	v_fma_f32 v175, v127, v203, v175
	v_fma_f32 v176, v120, v204, v176
	v_fma_f32 v177, v121, v205, v177
	v_fma_f32 v178, v122, v206, v178
	v_fma_f32 v179, v123, v207, v179
	v_cvt_pk_bf16_f32 v172, v172, v173
	v_cvt_pk_bf16_f32 v173, v174, v175
	v_cvt_pk_bf16_f32 v174, v176, v177
	v_cvt_pk_bf16_f32 v175, v178, v179
	s_mov_b32 s30, 0x40000
	s_mov_b32 s31, 0
	v_lshl_add_u64 v[222:223], v[218:219], 0, s[30:31]
	s_nop 1
	v_permlane32_swap_b32_e32 v172, v174
	v_permlane32_swap_b32_e32 v173, v175
	s_nop 1
	v_permlane16_swap_b32_e32 v172, v174
	v_permlane16_swap_b32_e32 v173, v175
	global_store_dwordx4 v[222:223], v[172:175], off
	s_mov_b32 s30, 0x200000
	s_mov_b32 s31, 0
	v_lshl_add_u64 v[220:221], v[216:217], 0, s[30:31]
	global_load_dwordx4 v[172:175], v[220:221], off offset:512 nt
	global_load_dwordx4 v[176:179], v[220:221], off offset:576 nt
	s_waitcnt vmcnt(12)
	v_fma_f32 v0, v108, v208, v0
	v_fma_f32 v1, v109, v209, v1
	v_fma_f32 v2, v110, v210, v2
	v_fma_f32 v3, v111, v211, v3
	v_fma_f32 v4, v104, v212, v4
	v_fma_f32 v5, v105, v213, v5
	v_fma_f32 v6, v106, v214, v6
	v_fma_f32 v7, v107, v215, v7
	v_cvt_pk_bf16_f32 v0, v0, v1
	v_cvt_pk_bf16_f32 v1, v2, v3
	v_cvt_pk_bf16_f32 v2, v4, v5
	v_cvt_pk_bf16_f32 v3, v6, v7
	s_mov_b32 s30, 0x40000
	s_mov_b32 s31, 0
	v_lshl_add_u64 v[222:223], v[218:219], 0, s[30:31]
	s_nop 1
	v_permlane32_swap_b32_e32 v0, v2
	v_permlane32_swap_b32_e32 v1, v3
	s_nop 1
	v_permlane16_swap_b32_e32 v0, v2
	v_permlane16_swap_b32_e32 v1, v3
	global_store_dwordx4 v[222:223], v[0:3], off offset:256
	s_mov_b32 s30, 0x240000
	s_mov_b32 s31, 0
	v_lshl_add_u64 v[220:221], v[216:217], 0, s[30:31]
	global_load_dwordx4 v[0:3], v[220:221], off nt
	global_load_dwordx4 v[4:7], v[220:221], off offset:64 nt
	s_waitcnt vmcnt(12)
	v_fma_f32 v8, v116, v200, v8
	v_fma_f32 v9, v117, v201, v9
	v_fma_f32 v10, v118, v202, v10
	v_fma_f32 v11, v119, v203, v11
	v_fma_f32 v12, v112, v204, v12
	v_fma_f32 v13, v113, v205, v13
	v_fma_f32 v14, v114, v206, v14
	v_fma_f32 v15, v115, v207, v15
	v_cvt_pk_bf16_f32 v8, v8, v9
	v_cvt_pk_bf16_f32 v9, v10, v11
	v_cvt_pk_bf16_f32 v10, v12, v13
	v_cvt_pk_bf16_f32 v11, v14, v15
	s_mov_b32 s30, 0x60000
	s_mov_b32 s31, 0
	v_lshl_add_u64 v[222:223], v[218:219], 0, s[30:31]
	s_nop 1
	v_permlane32_swap_b32_e32 v8, v10
	v_permlane32_swap_b32_e32 v9, v11
	s_nop 1
	v_permlane16_swap_b32_e32 v8, v10
	v_permlane16_swap_b32_e32 v9, v11
	global_store_dwordx4 v[222:223], v[8:11], off
	s_mov_b32 s30, 0x240000
	s_mov_b32 s31, 0
	v_lshl_add_u64 v[220:221], v[216:217], 0, s[30:31]
	global_load_dwordx4 v[8:11], v[220:221], off offset:512 nt
	global_load_dwordx4 v[12:15], v[220:221], off offset:576 nt
	s_waitcnt vmcnt(12)
	v_fma_f32 v16, v100, v208, v16
	v_fma_f32 v17, v101, v209, v17
	v_fma_f32 v18, v102, v210, v18
	v_fma_f32 v19, v103, v211, v19
	v_fma_f32 v20, v96, v212, v20
	v_fma_f32 v21, v97, v213, v21
	v_fma_f32 v22, v98, v214, v22
	v_fma_f32 v23, v99, v215, v23
	v_cvt_pk_bf16_f32 v16, v16, v17
	v_cvt_pk_bf16_f32 v17, v18, v19
	v_cvt_pk_bf16_f32 v18, v20, v21
	v_cvt_pk_bf16_f32 v19, v22, v23
	s_mov_b32 s30, 0x60000
	s_mov_b32 s31, 0
	v_lshl_add_u64 v[222:223], v[218:219], 0, s[30:31]
	s_nop 1
	v_permlane32_swap_b32_e32 v16, v18
	v_permlane32_swap_b32_e32 v17, v19
	s_nop 1
	v_permlane16_swap_b32_e32 v16, v18
	v_permlane16_swap_b32_e32 v17, v19
	global_store_dwordx4 v[222:223], v[16:19], off offset:256
	s_mov_b32 s30, 0x280000
	s_mov_b32 s31, 0
	v_lshl_add_u64 v[220:221], v[216:217], 0, s[30:31]
	global_load_dwordx4 v[16:19], v[220:221], off nt
	global_load_dwordx4 v[20:23], v[220:221], off offset:64 nt
	s_waitcnt vmcnt(12)
	v_fma_f32 v24, v92, v200, v24
	v_fma_f32 v25, v93, v201, v25
	v_fma_f32 v26, v94, v202, v26
	v_fma_f32 v27, v95, v203, v27
	v_fma_f32 v28, v88, v204, v28
	v_fma_f32 v29, v89, v205, v29
	v_fma_f32 v30, v90, v206, v30
	v_fma_f32 v31, v91, v207, v31
	v_cvt_pk_bf16_f32 v24, v24, v25
	v_cvt_pk_bf16_f32 v25, v26, v27
	v_cvt_pk_bf16_f32 v26, v28, v29
	v_cvt_pk_bf16_f32 v27, v30, v31
	s_mov_b32 s30, 0x100000
	s_mov_b32 s31, 0
	v_lshl_add_u64 v[222:223], v[218:219], 0, s[30:31]
	s_nop 1
	v_permlane32_swap_b32_e32 v24, v26
	v_permlane32_swap_b32_e32 v25, v27
	s_nop 1
	v_permlane16_swap_b32_e32 v24, v26
	v_permlane16_swap_b32_e32 v25, v27
	global_store_dwordx4 v[222:223], v[24:27], off
	s_mov_b32 s30, 0x280000
	s_mov_b32 s31, 0
	v_lshl_add_u64 v[220:221], v[216:217], 0, s[30:31]
	global_load_dwordx4 v[24:27], v[220:221], off offset:512 nt
	global_load_dwordx4 v[28:31], v[220:221], off offset:576 nt
	s_waitcnt vmcnt(12)
	v_fma_f32 v172, v76, v208, v172
	v_fma_f32 v173, v77, v209, v173
	v_fma_f32 v174, v78, v210, v174
	v_fma_f32 v175, v79, v211, v175
	v_fma_f32 v176, v72, v212, v176
	v_fma_f32 v177, v73, v213, v177
	v_fma_f32 v178, v74, v214, v178
	v_fma_f32 v179, v75, v215, v179
	v_cvt_pk_bf16_f32 v172, v172, v173
	v_cvt_pk_bf16_f32 v173, v174, v175
	v_cvt_pk_bf16_f32 v174, v176, v177
	v_cvt_pk_bf16_f32 v175, v178, v179
	s_mov_b32 s30, 0x100000
	s_mov_b32 s31, 0
	v_lshl_add_u64 v[222:223], v[218:219], 0, s[30:31]
	s_nop 1
	v_permlane32_swap_b32_e32 v172, v174
	v_permlane32_swap_b32_e32 v173, v175
	s_nop 1
	v_permlane16_swap_b32_e32 v172, v174
	v_permlane16_swap_b32_e32 v173, v175
	global_store_dwordx4 v[222:223], v[172:175], off offset:256
	s_mov_b32 s30, 0x2c0000
	s_mov_b32 s31, 0
	v_lshl_add_u64 v[220:221], v[216:217], 0, s[30:31]
	global_load_dwordx4 v[172:175], v[220:221], off nt
	global_load_dwordx4 v[176:179], v[220:221], off offset:64 nt
	s_waitcnt vmcnt(12)
	v_fma_f32 v0, v84, v200, v0
	v_fma_f32 v1, v85, v201, v1
	v_fma_f32 v2, v86, v202, v2
	v_fma_f32 v3, v87, v203, v3
	v_fma_f32 v4, v80, v204, v4
	v_fma_f32 v5, v81, v205, v5
	v_fma_f32 v6, v82, v206, v6
	v_fma_f32 v7, v83, v207, v7
	v_cvt_pk_bf16_f32 v0, v0, v1
	v_cvt_pk_bf16_f32 v1, v2, v3
	v_cvt_pk_bf16_f32 v2, v4, v5
	v_cvt_pk_bf16_f32 v3, v6, v7
	s_mov_b32 s30, 0x120000
	s_mov_b32 s31, 0
	v_lshl_add_u64 v[222:223], v[218:219], 0, s[30:31]
	s_nop 1
	v_permlane32_swap_b32_e32 v0, v2
	v_permlane32_swap_b32_e32 v1, v3
	s_nop 1
	v_permlane16_swap_b32_e32 v0, v2
	v_permlane16_swap_b32_e32 v1, v3
	global_store_dwordx4 v[222:223], v[0:3], off
	s_mov_b32 s30, 0x2c0000
	s_mov_b32 s31, 0
	v_lshl_add_u64 v[220:221], v[216:217], 0, s[30:31]
	global_load_dwordx4 v[0:3], v[220:221], off offset:512 nt
	global_load_dwordx4 v[4:7], v[220:221], off offset:576 nt
	s_waitcnt vmcnt(12)
	v_fma_f32 v8, v68, v208, v8
	v_fma_f32 v9, v69, v209, v9
	v_fma_f32 v10, v70, v210, v10
	v_fma_f32 v11, v71, v211, v11
	v_fma_f32 v12, v64, v212, v12
	v_fma_f32 v13, v65, v213, v13
	v_fma_f32 v14, v66, v214, v14
	v_fma_f32 v15, v67, v215, v15
	v_cvt_pk_bf16_f32 v8, v8, v9
	v_cvt_pk_bf16_f32 v9, v10, v11
	v_cvt_pk_bf16_f32 v10, v12, v13
	v_cvt_pk_bf16_f32 v11, v14, v15
	s_mov_b32 s30, 0x120000
	s_mov_b32 s31, 0
	v_lshl_add_u64 v[222:223], v[218:219], 0, s[30:31]
	s_nop 1
	v_permlane32_swap_b32_e32 v8, v10
	v_permlane32_swap_b32_e32 v9, v11
	s_nop 1
	v_permlane16_swap_b32_e32 v8, v10
	v_permlane16_swap_b32_e32 v9, v11
	global_store_dwordx4 v[222:223], v[8:11], off offset:256
	s_waitcnt vmcnt(10)
	v_fma_f32 v16, v60, v200, v16
	v_fma_f32 v17, v61, v201, v17
	v_fma_f32 v18, v62, v202, v18
	v_fma_f32 v19, v63, v203, v19
	v_fma_f32 v20, v56, v204, v20
	v_fma_f32 v21, v57, v205, v21
	v_fma_f32 v22, v58, v206, v22
	v_fma_f32 v23, v59, v207, v23
	v_cvt_pk_bf16_f32 v16, v16, v17
	v_cvt_pk_bf16_f32 v17, v18, v19
	v_cvt_pk_bf16_f32 v18, v20, v21
	v_cvt_pk_bf16_f32 v19, v22, v23
	s_mov_b32 s30, 0x140000
	s_mov_b32 s31, 0
	v_lshl_add_u64 v[222:223], v[218:219], 0, s[30:31]
	s_nop 1
	v_permlane32_swap_b32_e32 v16, v18
	v_permlane32_swap_b32_e32 v17, v19
	s_nop 1
	v_permlane16_swap_b32_e32 v16, v18
	v_permlane16_swap_b32_e32 v17, v19
	global_store_dwordx4 v[222:223], v[16:19], off
	s_waitcnt vmcnt(8)
	v_fma_f32 v24, v44, v208, v24
	v_fma_f32 v25, v45, v209, v25
	v_fma_f32 v26, v46, v210, v26
	v_fma_f32 v27, v47, v211, v27
	v_fma_f32 v28, v40, v212, v28
	v_fma_f32 v29, v41, v213, v29
	v_fma_f32 v30, v42, v214, v30
	v_fma_f32 v31, v43, v215, v31
	v_cvt_pk_bf16_f32 v24, v24, v25
	v_cvt_pk_bf16_f32 v25, v26, v27
	v_cvt_pk_bf16_f32 v26, v28, v29
	v_cvt_pk_bf16_f32 v27, v30, v31
	s_mov_b32 s30, 0x140000
	s_mov_b32 s31, 0
	v_lshl_add_u64 v[222:223], v[218:219], 0, s[30:31]
	s_nop 1
	v_permlane32_swap_b32_e32 v24, v26
	v_permlane32_swap_b32_e32 v25, v27
	s_nop 1
	v_permlane16_swap_b32_e32 v24, v26
	v_permlane16_swap_b32_e32 v25, v27
	global_store_dwordx4 v[222:223], v[24:27], off offset:256
	s_waitcnt vmcnt(6)
	v_fma_f32 v172, v52, v200, v172
	v_fma_f32 v173, v53, v201, v173
	v_fma_f32 v174, v54, v202, v174
	v_fma_f32 v175, v55, v203, v175
	v_fma_f32 v176, v48, v204, v176
	v_fma_f32 v177, v49, v205, v177
	v_fma_f32 v178, v50, v206, v178
	v_fma_f32 v179, v51, v207, v179
	v_cvt_pk_bf16_f32 v172, v172, v173
	v_cvt_pk_bf16_f32 v173, v174, v175
	v_cvt_pk_bf16_f32 v174, v176, v177
	v_cvt_pk_bf16_f32 v175, v178, v179
	s_mov_b32 s30, 0x160000
	s_mov_b32 s31, 0
	v_lshl_add_u64 v[222:223], v[218:219], 0, s[30:31]
	s_nop 1
	v_permlane32_swap_b32_e32 v172, v174
	v_permlane32_swap_b32_e32 v173, v175
	s_nop 1
	v_permlane16_swap_b32_e32 v172, v174
	v_permlane16_swap_b32_e32 v173, v175
	global_store_dwordx4 v[222:223], v[172:175], off
	s_waitcnt vmcnt(4)
	v_fma_f32 v0, v36, v208, v0
	v_fma_f32 v1, v37, v209, v1
	v_fma_f32 v2, v38, v210, v2
	v_fma_f32 v3, v39, v211, v3
	v_fma_f32 v4, v32, v212, v4
	v_fma_f32 v5, v33, v213, v5
	v_fma_f32 v6, v34, v214, v6
	v_fma_f32 v7, v35, v215, v7
	v_cvt_pk_bf16_f32 v0, v0, v1
	v_cvt_pk_bf16_f32 v1, v2, v3
	v_cvt_pk_bf16_f32 v2, v4, v5
	v_cvt_pk_bf16_f32 v3, v6, v7
	s_mov_b32 s30, 0x160000
	s_mov_b32 s31, 0
	v_lshl_add_u64 v[222:223], v[218:219], 0, s[30:31]
	s_nop 1
	v_permlane32_swap_b32_e32 v0, v2
	v_permlane32_swap_b32_e32 v1, v3
	s_nop 1
	v_permlane16_swap_b32_e32 v0, v2
	v_permlane16_swap_b32_e32 v1, v3
	global_store_dwordx4 v[222:223], v[0:3], off offset:256
	s_cbranch_vccnz .LBB0_554
	s_andn2_b64 vcc, exec, s[10:11]
	s_cbranch_vccnz .LBB0_553
	s_barrier
	s_branch .LBB0_553

.LBB0_1361:
	s_andn2_b64 vcc, exec, s[0:1]
	s_mov_b64 s[0:1], -1
	s_ashr_i32 s17, s24, 4
	s_mul_hi_i32 s19, s17, 0x18000
	s_mul_i32 s17, s17, 0x18000
	s_add_u32 s26, s45, s17
	s_addc_u32 s27, s46, s19
	v_lshl_or_b32 v238, s54, 8, v223
	v_mov_b32_e32 v239, 0
	v_lshl_add_u64 v[240:241], v[238:239], 2, s[26:27]
	global_load_dwordx4 v[176:179], v[240:241], off
	global_load_dwordx4 v[180:183], v[240:241], off offset:64
	global_load_dwordx4 v[184:187], v[240:241], off offset:512
	global_load_dwordx4 v[188:191], v[240:241], off offset:576
	v_lshl_add_u32 v242, s24, 8, v206
	v_mov_b32_e32 v243, 0
	v_lshlrev_b64 v[192:193], 13, v[242:243]
	v_lshl_add_u64 v[192:193], v[192:193], 0, s[8:9]
	v_and_b32_e32 v244, 12, v223
	v_add_u32_e32 v244, v244, v238
	v_mov_b32_e32 v245, 0
	v_lshl_add_u64 v[192:193], v[244:245], 1, v[192:193]
	v_and_b32_e32 v242, -9, v206
	v_lshl_add_u32 v242, s24, 8, v242
	v_lshlrev_b64 v[194:195], 14, v[242:243]
	v_lshl_add_u64 v[194:195], v[194:195], 0, s[4:5]
	v_lshl_add_u64 v[194:195], v[238:239], 2, v[194:195]
	v_and_b32_e32 v244, 8, v206
	v_lshlrev_b32_e32 v244, 3, v244
	v_lshl_add_u64 v[194:195], v[244:245], 0, v[194:195]
	s_mov_b32 s26, 0x0
	s_mov_b32 s27, 0
	v_lshl_add_u64 v[196:197], v[192:193], 0, s[26:27]
	global_load_dwordx4 v[0:3], v[196:197], off nt
	s_mov_b32 s26, 0x0
	s_mov_b32 s27, 0
	v_lshl_add_u64 v[196:197], v[192:193], 0, s[26:27]
	global_load_dwordx4 v[4:7], v[196:197], off offset:256 nt
	s_mov_b32 s26, 0x20000
	s_mov_b32 s27, 0
	v_lshl_add_u64 v[196:197], v[192:193], 0, s[26:27]
	global_load_dwordx4 v[8:11], v[196:197], off nt
	s_mov_b32 s26, 0x20000
	s_mov_b32 s27, 0
	v_lshl_add_u64 v[196:197], v[192:193], 0, s[26:27]
	global_load_dwordx4 v[12:15], v[196:197], off offset:256 nt
	s_mov_b32 s26, 0x40000
	s_mov_b32 s27, 0
	v_lshl_add_u64 v[196:197], v[192:193], 0, s[26:27]
	global_load_dwordx4 v[16:19], v[196:197], off nt
	s_mov_b32 s26, 0x40000
	s_mov_b32 s27, 0
	v_lshl_add_u64 v[196:197], v[192:193], 0, s[26:27]
	global_load_dwordx4 v[20:23], v[196:197], off offset:256 nt
	s_mov_b32 s26, 0x60000
	s_mov_b32 s27, 0
	v_lshl_add_u64 v[196:197], v[192:193], 0, s[26:27]
	global_load_dwordx4 v[24:27], v[196:197], off nt
	s_mov_b32 s26, 0x60000
	s_mov_b32 s27, 0
	v_lshl_add_u64 v[196:197], v[192:193], 0, s[26:27]
	global_load_dwordx4 v[28:31], v[196:197], off offset:256 nt
	s_waitcnt vmcnt(8)
	v_mul_f32_e32 v176, s14, v176
	v_mul_f32_e32 v177, s14, v177
	v_mul_f32_e32 v178, s14, v178
	v_mul_f32_e32 v179, s14, v179
	v_mul_f32_e32 v180, s14, v180
	v_mul_f32_e32 v181, s14, v181
	v_mul_f32_e32 v182, s14, v182
	v_mul_f32_e32 v183, s14, v183
	v_mul_f32_e32 v184, s14, v184
	v_mul_f32_e32 v185, s14, v185
	v_mul_f32_e32 v186, s14, v186
	v_mul_f32_e32 v187, s14, v187
	v_mul_f32_e32 v188, s14, v188
	v_mul_f32_e32 v189, s14, v189
	v_mul_f32_e32 v190, s14, v190
	v_mul_f32_e32 v191, s14, v191
	s_waitcnt vmcnt(7)
	v_permlane16_swap_b32_e32 v0, v2
	v_permlane16_swap_b32_e32 v1, v3
	s_nop 1
	v_permlane32_swap_b32_e32 v0, v2
	v_permlane32_swap_b32_e32 v1, v3
	s_nop 1
	v_lshlrev_b32_e32 v226, 16, v0
	v_and_b32_e32 v227, 0xffff0000, v0
	v_lshlrev_b32_e32 v228, 16, v1
	v_and_b32_e32 v229, 0xffff0000, v1
	v_lshlrev_b32_e32 v230, 16, v2
	v_and_b32_e32 v231, 0xffff0000, v2
	v_lshlrev_b32_e32 v232, 16, v3
	v_and_b32_e32 v233, 0xffff0000, v3
	v_fma_f32 v226, v156, v176, v226
	v_fma_f32 v227, v157, v177, v227
	v_fma_f32 v228, v158, v178, v228
	v_fma_f32 v229, v159, v179, v229
	v_fma_f32 v230, v152, v180, v230
	v_fma_f32 v231, v153, v181, v231
	v_fma_f32 v232, v154, v182, v232
	v_fma_f32 v233, v155, v183, v233
	v_mov_b32_e32 v234, v230
	v_mov_b32_e32 v235, v231
	v_mov_b32_e32 v236, v232
	v_mov_b32_e32 v237, v233
	s_mov_b32 s26, 0x0
	s_mov_b32 s27, 0
	v_lshl_add_u64 v[198:199], v[194:195], 0, s[26:27]
	v_mov_b32_dpp v230, v226 row_ror:8 row_mask:0xf bank_mask:0x3
	v_mov_b32_dpp v231, v227 row_ror:8 row_mask:0xf bank_mask:0x3
	v_mov_b32_dpp v232, v228 row_ror:8 row_mask:0xf bank_mask:0x3
	v_mov_b32_dpp v233, v229 row_ror:8 row_mask:0xf bank_mask:0x3
	v_mov_b32_dpp v226, v234 row_ror:8 row_mask:0xf bank_mask:0xc
	v_mov_b32_dpp v227, v235 row_ror:8 row_mask:0xf bank_mask:0xc
	v_mov_b32_dpp v228, v236 row_ror:8 row_mask:0xf bank_mask:0xc
	v_mov_b32_dpp v229, v237 row_ror:8 row_mask:0xf bank_mask:0xc
	global_store_dwordx4 v[198:199], v[226:229], off nt
	s_mov_b32 s26, 0x20000
	s_mov_b32 s27, 0
	v_lshl_add_u64 v[198:199], v[198:199], 0, s[26:27]
	global_store_dwordx4 v[198:199], v[230:233], off nt
	s_nop 1
	s_mov_b32 s26, 0x100000
	s_mov_b32 s27, 0
	v_lshl_add_u64 v[196:197], v[192:193], 0, s[26:27]
	global_load_dwordx4 v[0:3], v[196:197], off nt
	s_waitcnt vmcnt(9)
	v_permlane16_swap_b32_e32 v4, v6
	v_permlane16_swap_b32_e32 v5, v7
	s_nop 1
	v_permlane32_swap_b32_e32 v4, v6
	v_permlane32_swap_b32_e32 v5, v7
	s_nop 1
	v_lshlrev_b32_e32 v226, 16, v4
	v_and_b32_e32 v227, 0xffff0000, v4
	v_lshlrev_b32_e32 v228, 16, v5
	v_and_b32_e32 v229, 0xffff0000, v5
	v_lshlrev_b32_e32 v230, 16, v6
	v_and_b32_e32 v231, 0xffff0000, v6
	v_lshlrev_b32_e32 v232, 16, v7
	v_and_b32_e32 v233, 0xffff0000, v7
	v_fma_f32 v226, v148, v184, v226
	v_fma_f32 v227, v149, v185, v227
	v_fma_f32 v228, v150, v186, v228
	v_fma_f32 v229, v151, v187, v229
	v_fma_f32 v230, v140, v188, v230
	v_fma_f32 v231, v141, v189, v231
	v_fma_f32 v232, v142, v190, v232
	v_fma_f32 v233, v143, v191, v233
	v_mov_b32_e32 v234, v230
	v_mov_b32_e32 v235, v231
	v_mov_b32_e32 v236, v232
	v_mov_b32_e32 v237, v233
	s_mov_b32 s26, 0x0
	s_mov_b32 s27, 0
	v_lshl_add_u64 v[198:199], v[194:195], 0, s[26:27]
	v_mov_b32_dpp v230, v226 row_ror:8 row_mask:0xf bank_mask:0x3
	v_mov_b32_dpp v231, v227 row_ror:8 row_mask:0xf bank_mask:0x3
	v_mov_b32_dpp v232, v228 row_ror:8 row_mask:0xf bank_mask:0x3
	v_mov_b32_dpp v233, v229 row_ror:8 row_mask:0xf bank_mask:0x3
	v_mov_b32_dpp v226, v234 row_ror:8 row_mask:0xf bank_mask:0xc
	v_mov_b32_dpp v227, v235 row_ror:8 row_mask:0xf bank_mask:0xc
	v_mov_b32_dpp v228, v236 row_ror:8 row_mask:0xf bank_mask:0xc
	v_mov_b32_dpp v229, v237 row_ror:8 row_mask:0xf bank_mask:0xc
	global_store_dwordx4 v[198:199], v[226:229], off offset:512 nt
	s_mov_b32 s26, 0x20000
	s_mov_b32 s27, 0
	v_lshl_add_u64 v[198:199], v[198:199], 0, s[26:27]
	global_store_dwordx4 v[198:199], v[230:233], off offset:512 nt
	s_nop 1
	s_mov_b32 s26, 0x100000
	s_mov_b32 s27, 0
	v_lshl_add_u64 v[196:197], v[192:193], 0, s[26:27]
	global_load_dwordx4 v[4:7], v[196:197], off offset:256 nt
	s_waitcnt vmcnt(11)
	v_permlane16_swap_b32_e32 v8, v10
	v_permlane16_swap_b32_e32 v9, v11
	s_nop 1
	v_permlane32_swap_b32_e32 v8, v10
	v_permlane32_swap_b32_e32 v9, v11
	s_nop 1
	v_lshlrev_b32_e32 v226, 16, v8
	v_and_b32_e32 v227, 0xffff0000, v8
	v_lshlrev_b32_e32 v228, 16, v9
	v_and_b32_e32 v229, 0xffff0000, v9
	v_lshlrev_b32_e32 v230, 16, v10
	v_and_b32_e32 v231, 0xffff0000, v10
	v_lshlrev_b32_e32 v232, 16, v11
	v_and_b32_e32 v233, 0xffff0000, v11
	v_fma_f32 v226, v144, v176, v226
	v_fma_f32 v227, v145, v177, v227
	v_fma_f32 v228, v146, v178, v228
	v_fma_f32 v229, v147, v179, v229
	v_fma_f32 v230, v136, v180, v230
	v_fma_f32 v231, v137, v181, v231
	v_fma_f32 v232, v138, v182, v232
	v_fma_f32 v233, v139, v183, v233
	v_mov_b32_e32 v234, v230
	v_mov_b32_e32 v235, v231
	v_mov_b32_e32 v236, v232
	v_mov_b32_e32 v237, v233
	s_mov_b32 s26, 0x40000
	s_mov_b32 s27, 0
	v_lshl_add_u64 v[198:199], v[194:195], 0, s[26:27]
	v_mov_b32_dpp v230, v226 row_ror:8 row_mask:0xf bank_mask:0x3
	v_mov_b32_dpp v231, v227 row_ror:8 row_mask:0xf bank_mask:0x3
	v_mov_b32_dpp v232, v228 row_ror:8 row_mask:0xf bank_mask:0x3
	v_mov_b32_dpp v233, v229 row_ror:8 row_mask:0xf bank_mask:0x3
	v_mov_b32_dpp v226, v234 row_ror:8 row_mask:0xf bank_mask:0xc
	v_mov_b32_dpp v227, v235 row_ror:8 row_mask:0xf bank_mask:0xc
	v_mov_b32_dpp v228, v236 row_ror:8 row_mask:0xf bank_mask:0xc
	v_mov_b32_dpp v229, v237 row_ror:8 row_mask:0xf bank_mask:0xc
	global_store_dwordx4 v[198:199], v[226:229], off nt
	s_mov_b32 s26, 0x20000
	s_mov_b32 s27, 0
	v_lshl_add_u64 v[198:199], v[198:199], 0, s[26:27]
	global_store_dwordx4 v[198:199], v[230:233], off nt
	s_nop 1
	s_mov_b32 s26, 0x120000
	s_mov_b32 s27, 0
	v_lshl_add_u64 v[196:197], v[192:193], 0, s[26:27]
	global_load_dwordx4 v[8:11], v[196:197], off nt
	s_waitcnt vmcnt(13)
	v_permlane16_swap_b32_e32 v12, v14
	v_permlane16_swap_b32_e32 v13, v15
	s_nop 1
	v_permlane32_swap_b32_e32 v12, v14
	v_permlane32_swap_b32_e32 v13, v15
	s_nop 1
	v_lshlrev_b32_e32 v226, 16, v12
	v_and_b32_e32 v227, 0xffff0000, v12
	v_lshlrev_b32_e32 v228, 16, v13
	v_and_b32_e32 v229, 0xffff0000, v13
	v_lshlrev_b32_e32 v230, 16, v14
	v_and_b32_e32 v231, 0xffff0000, v14
	v_lshlrev_b32_e32 v232, 16, v15
	v_and_b32_e32 v233, 0xffff0000, v15
	v_fma_f32 v226, v132, v184, v226
	v_fma_f32 v227, v133, v185, v227
	v_fma_f32 v228, v134, v186, v228
	v_fma_f32 v229, v135, v187, v229
	v_fma_f32 v230, v128, v188, v230
	v_fma_f32 v231, v129, v189, v231
	v_fma_f32 v232, v130, v190, v232
	v_fma_f32 v233, v131, v191, v233
	v_mov_b32_e32 v234, v230
	v_mov_b32_e32 v235, v231
	v_mov_b32_e32 v236, v232
	v_mov_b32_e32 v237, v233
	s_mov_b32 s26, 0x40000
	s_mov_b32 s27, 0
	v_lshl_add_u64 v[198:199], v[194:195], 0, s[26:27]
	v_mov_b32_dpp v230, v226 row_ror:8 row_mask:0xf bank_mask:0x3
	v_mov_b32_dpp v231, v227 row_ror:8 row_mask:0xf bank_mask:0x3
	v_mov_b32_dpp v232, v228 row_ror:8 row_mask:0xf bank_mask:0x3
	v_mov_b32_dpp v233, v229 row_ror:8 row_mask:0xf bank_mask:0x3
	v_mov_b32_dpp v226, v234 row_ror:8 row_mask:0xf bank_mask:0xc
	v_mov_b32_dpp v227, v235 row_ror:8 row_mask:0xf bank_mask:0xc
	v_mov_b32_dpp v228, v236 row_ror:8 row_mask:0xf bank_mask:0xc
	v_mov_b32_dpp v229, v237 row_ror:8 row_mask:0xf bank_mask:0xc
	global_store_dwordx4 v[198:199], v[226:229], off offset:512 nt
	s_mov_b32 s26, 0x20000
	s_mov_b32 s27, 0
	v_lshl_add_u64 v[198:199], v[198:199], 0, s[26:27]
	global_store_dwordx4 v[198:199], v[230:233], off offset:512 nt
	s_nop 1
	s_mov_b32 s26, 0x120000
	s_mov_b32 s27, 0
	v_lshl_add_u64 v[196:197], v[192:193], 0, s[26:27]
	global_load_dwordx4 v[12:15], v[196:197], off offset:256 nt
	s_waitcnt vmcnt(15)
	v_permlane16_swap_b32_e32 v16, v18
	v_permlane16_swap_b32_e32 v17, v19
	s_nop 1
	v_permlane32_swap_b32_e32 v16, v18
	v_permlane32_swap_b32_e32 v17, v19
	s_nop 1
	v_lshlrev_b32_e32 v226, 16, v16
	v_and_b32_e32 v227, 0xffff0000, v16
	v_lshlrev_b32_e32 v228, 16, v17
	v_and_b32_e32 v229, 0xffff0000, v17
	v_lshlrev_b32_e32 v230, 16, v18
	v_and_b32_e32 v231, 0xffff0000, v18
	v_lshlrev_b32_e32 v232, 16, v19
	v_and_b32_e32 v233, 0xffff0000, v19
	v_fma_f32 v226, v124, v176, v226
	v_fma_f32 v227, v125, v177, v227
	v_fma_f32 v228, v126, v178, v228
	v_fma_f32 v229, v127, v179, v229
	v_fma_f32 v230, v120, v180, v230
	v_fma_f32 v231, v121, v181, v231
	v_fma_f32 v232, v122, v182, v232
	v_fma_f32 v233, v123, v183, v233
	v_mov_b32_e32 v234, v230
	v_mov_b32_e32 v235, v231
	v_mov_b32_e32 v236, v232
	v_mov_b32_e32 v237, v233
	s_mov_b32 s26, 0x80000
	s_mov_b32 s27, 0
	v_lshl_add_u64 v[198:199], v[194:195], 0, s[26:27]
	v_mov_b32_dpp v230, v226 row_ror:8 row_mask:0xf bank_mask:0x3
	v_mov_b32_dpp v231, v227 row_ror:8 row_mask:0xf bank_mask:0x3
	v_mov_b32_dpp v232, v228 row_ror:8 row_mask:0xf bank_mask:0x3
	v_mov_b32_dpp v233, v229 row_ror:8 row_mask:0xf bank_mask:0x3
	v_mov_b32_dpp v226, v234 row_ror:8 row_mask:0xf bank_mask:0xc
	v_mov_b32_dpp v227, v235 row_ror:8 row_mask:0xf bank_mask:0xc
	v_mov_b32_dpp v228, v236 row_ror:8 row_mask:0xf bank_mask:0xc
	v_mov_b32_dpp v229, v237 row_ror:8 row_mask:0xf bank_mask:0xc
	global_store_dwordx4 v[198:199], v[226:229], off nt
	s_mov_b32 s26, 0x20000
	s_mov_b32 s27, 0
	v_lshl_add_u64 v[198:199], v[198:199], 0, s[26:27]
	global_store_dwordx4 v[198:199], v[230:233], off nt
	s_nop 1
	s_mov_b32 s26, 0x140000
	s_mov_b32 s27, 0
	v_lshl_add_u64 v[196:197], v[192:193], 0, s[26:27]
	global_load_dwordx4 v[16:19], v[196:197], off nt
	s_waitcnt vmcnt(17)
	v_permlane16_swap_b32_e32 v20, v22
	v_permlane16_swap_b32_e32 v21, v23
	s_nop 1
	v_permlane32_swap_b32_e32 v20, v22
	v_permlane32_swap_b32_e32 v21, v23
	s_nop 1
	v_lshlrev_b32_e32 v226, 16, v20
	v_and_b32_e32 v227, 0xffff0000, v20
	v_lshlrev_b32_e32 v228, 16, v21
	v_and_b32_e32 v229, 0xffff0000, v21
	v_lshlrev_b32_e32 v230, 16, v22
	v_and_b32_e32 v231, 0xffff0000, v22
	v_lshlrev_b32_e32 v232, 16, v23
	v_and_b32_e32 v233, 0xffff0000, v23
	v_fma_f32 v226, v116, v184, v226
	v_fma_f32 v227, v117, v185, v227
	v_fma_f32 v228, v118, v186, v228
	v_fma_f32 v229, v119, v187, v229
	v_fma_f32 v230, v108, v188, v230
	v_fma_f32 v231, v109, v189, v231
	v_fma_f32 v232, v110, v190, v232
	v_fma_f32 v233, v111, v191, v233
	v_mov_b32_e32 v234, v230
	v_mov_b32_e32 v235, v231
	v_mov_b32_e32 v236, v232
	v_mov_b32_e32 v237, v233
	s_mov_b32 s26, 0x80000
	s_mov_b32 s27, 0
	v_lshl_add_u64 v[198:199], v[194:195], 0, s[26:27]
	v_mov_b32_dpp v230, v226 row_ror:8 row_mask:0xf bank_mask:0x3
	v_mov_b32_dpp v231, v227 row_ror:8 row_mask:0xf bank_mask:0x3
	v_mov_b32_dpp v232, v228 row_ror:8 row_mask:0xf bank_mask:0x3
	v_mov_b32_dpp v233, v229 row_ror:8 row_mask:0xf bank_mask:0x3
	v_mov_b32_dpp v226, v234 row_ror:8 row_mask:0xf bank_mask:0xc
	v_mov_b32_dpp v227, v235 row_ror:8 row_mask:0xf bank_mask:0xc
	v_mov_b32_dpp v228, v236 row_ror:8 row_mask:0xf bank_mask:0xc
	v_mov_b32_dpp v229, v237 row_ror:8 row_mask:0xf bank_mask:0xc
	global_store_dwordx4 v[198:199], v[226:229], off offset:512 nt
	s_mov_b32 s26, 0x20000
	s_mov_b32 s27, 0
	v_lshl_add_u64 v[198:199], v[198:199], 0, s[26:27]
	global_store_dwordx4 v[198:199], v[230:233], off offset:512 nt
	s_nop 1
	s_mov_b32 s26, 0x140000
	s_mov_b32 s27, 0
	v_lshl_add_u64 v[196:197], v[192:193], 0, s[26:27]
	global_load_dwordx4 v[20:23], v[196:197], off offset:256 nt
	s_waitcnt vmcnt(19)
	v_permlane16_swap_b32_e32 v24, v26
	v_permlane16_swap_b32_e32 v25, v27
	s_nop 1
	v_permlane32_swap_b32_e32 v24, v26
	v_permlane32_swap_b32_e32 v25, v27
	s_nop 1
	v_lshlrev_b32_e32 v226, 16, v24
	v_and_b32_e32 v227, 0xffff0000, v24
	v_lshlrev_b32_e32 v228, 16, v25
	v_and_b32_e32 v229, 0xffff0000, v25
	v_lshlrev_b32_e32 v230, 16, v26
	v_and_b32_e32 v231, 0xffff0000, v26
	v_lshlrev_b32_e32 v232, 16, v27
	v_and_b32_e32 v233, 0xffff0000, v27
	v_fma_f32 v226, v112, v176, v226
	v_fma_f32 v227, v113, v177, v227
	v_fma_f32 v228, v114, v178, v228
	v_fma_f32 v229, v115, v179, v229
	v_fma_f32 v230, v104, v180, v230
	v_fma_f32 v231, v105, v181, v231
	v_fma_f32 v232, v106, v182, v232
	v_fma_f32 v233, v107, v183, v233
	v_mov_b32_e32 v234, v230
	v_mov_b32_e32 v235, v231
	v_mov_b32_e32 v236, v232
	v_mov_b32_e32 v237, v233
	s_mov_b32 s26, 0xc0000
	s_mov_b32 s27, 0
	v_lshl_add_u64 v[198:199], v[194:195], 0, s[26:27]
	v_mov_b32_dpp v230, v226 row_ror:8 row_mask:0xf bank_mask:0x3
	v_mov_b32_dpp v231, v227 row_ror:8 row_mask:0xf bank_mask:0x3
	v_mov_b32_dpp v232, v228 row_ror:8 row_mask:0xf bank_mask:0x3
	v_mov_b32_dpp v233, v229 row_ror:8 row_mask:0xf bank_mask:0x3
	v_mov_b32_dpp v226, v234 row_ror:8 row_mask:0xf bank_mask:0xc
	v_mov_b32_dpp v227, v235 row_ror:8 row_mask:0xf bank_mask:0xc
	v_mov_b32_dpp v228, v236 row_ror:8 row_mask:0xf bank_mask:0xc
	v_mov_b32_dpp v229, v237 row_ror:8 row_mask:0xf bank_mask:0xc
	global_store_dwordx4 v[198:199], v[226:229], off nt
	s_mov_b32 s26, 0x20000
	s_mov_b32 s27, 0
	v_lshl_add_u64 v[198:199], v[198:199], 0, s[26:27]
	global_store_dwordx4 v[198:199], v[230:233], off nt
	s_nop 1
	s_mov_b32 s26, 0x160000
	s_mov_b32 s27, 0
	v_lshl_add_u64 v[196:197], v[192:193], 0, s[26:27]
	global_load_dwordx4 v[24:27], v[196:197], off nt
	s_waitcnt vmcnt(21)
	v_permlane16_swap_b32_e32 v28, v30
	v_permlane16_swap_b32_e32 v29, v31
	s_nop 1
	v_permlane32_swap_b32_e32 v28, v30
	v_permlane32_swap_b32_e32 v29, v31
	s_nop 1
	v_lshlrev_b32_e32 v226, 16, v28
	v_and_b32_e32 v227, 0xffff0000, v28
	v_lshlrev_b32_e32 v228, 16, v29
	v_and_b32_e32 v229, 0xffff0000, v29
	v_lshlrev_b32_e32 v230, 16, v30
	v_and_b32_e32 v231, 0xffff0000, v30
	v_lshlrev_b32_e32 v232, 16, v31
	v_and_b32_e32 v233, 0xffff0000, v31
	v_fma_f32 v226, v100, v184, v226
	v_fma_f32 v227, v101, v185, v227
	v_fma_f32 v228, v102, v186, v228
	v_fma_f32 v229, v103, v187, v229
	v_fma_f32 v230, v96, v188, v230
	v_fma_f32 v231, v97, v189, v231
	v_fma_f32 v232, v98, v190, v232
	v_fma_f32 v233, v99, v191, v233
	v_mov_b32_e32 v234, v230
	v_mov_b32_e32 v235, v231
	v_mov_b32_e32 v236, v232
	v_mov_b32_e32 v237, v233
	s_mov_b32 s26, 0xc0000
	s_mov_b32 s27, 0
	v_lshl_add_u64 v[198:199], v[194:195], 0, s[26:27]
	v_mov_b32_dpp v230, v226 row_ror:8 row_mask:0xf bank_mask:0x3
	v_mov_b32_dpp v231, v227 row_ror:8 row_mask:0xf bank_mask:0x3
	v_mov_b32_dpp v232, v228 row_ror:8 row_mask:0xf bank_mask:0x3
	v_mov_b32_dpp v233, v229 row_ror:8 row_mask:0xf bank_mask:0x3
	v_mov_b32_dpp v226, v234 row_ror:8 row_mask:0xf bank_mask:0xc
	v_mov_b32_dpp v227, v235 row_ror:8 row_mask:0xf bank_mask:0xc
	v_mov_b32_dpp v228, v236 row_ror:8 row_mask:0xf bank_mask:0xc
	v_mov_b32_dpp v229, v237 row_ror:8 row_mask:0xf bank_mask:0xc
	global_store_dwordx4 v[198:199], v[226:229], off offset:512 nt
	s_mov_b32 s26, 0x20000
	s_mov_b32 s27, 0
	v_lshl_add_u64 v[198:199], v[198:199], 0, s[26:27]
	global_store_dwordx4 v[198:199], v[230:233], off offset:512 nt
	s_nop 1
	s_mov_b32 s26, 0x160000
	s_mov_b32 s27, 0
	v_lshl_add_u64 v[196:197], v[192:193], 0, s[26:27]
	global_load_dwordx4 v[28:31], v[196:197], off offset:256 nt
	s_waitcnt vmcnt(21)
	v_permlane16_swap_b32_e32 v0, v2
	v_permlane16_swap_b32_e32 v1, v3
	s_nop 1
	v_permlane32_swap_b32_e32 v0, v2
	v_permlane32_swap_b32_e32 v1, v3
	s_nop 1
	v_lshlrev_b32_e32 v226, 16, v0
	v_and_b32_e32 v227, 0xffff0000, v0
	v_lshlrev_b32_e32 v228, 16, v1
	v_and_b32_e32 v229, 0xffff0000, v1
	v_lshlrev_b32_e32 v230, 16, v2
	v_and_b32_e32 v231, 0xffff0000, v2
	v_lshlrev_b32_e32 v232, 16, v3
	v_and_b32_e32 v233, 0xffff0000, v3
	v_fma_f32 v226, v92, v176, v226
	v_fma_f32 v227, v93, v177, v227
	v_fma_f32 v228, v94, v178, v228
	v_fma_f32 v229, v95, v179, v229
	v_fma_f32 v230, v88, v180, v230
	v_fma_f32 v231, v89, v181, v231
	v_fma_f32 v232, v90, v182, v232
	v_fma_f32 v233, v91, v183, v233
	v_mov_b32_e32 v234, v230
	v_mov_b32_e32 v235, v231
	v_mov_b32_e32 v236, v232
	v_mov_b32_e32 v237, v233
	s_mov_b32 s26, 0x200000
	s_mov_b32 s27, 0
	v_lshl_add_u64 v[198:199], v[194:195], 0, s[26:27]
	v_mov_b32_dpp v230, v226 row_ror:8 row_mask:0xf bank_mask:0x3
	v_mov_b32_dpp v231, v227 row_ror:8 row_mask:0xf bank_mask:0x3
	v_mov_b32_dpp v232, v228 row_ror:8 row_mask:0xf bank_mask:0x3
	v_mov_b32_dpp v233, v229 row_ror:8 row_mask:0xf bank_mask:0x3
	v_mov_b32_dpp v226, v234 row_ror:8 row_mask:0xf bank_mask:0xc
	v_mov_b32_dpp v227, v235 row_ror:8 row_mask:0xf bank_mask:0xc
	v_mov_b32_dpp v228, v236 row_ror:8 row_mask:0xf bank_mask:0xc
	v_mov_b32_dpp v229, v237 row_ror:8 row_mask:0xf bank_mask:0xc
	global_store_dwordx4 v[198:199], v[226:229], off nt
	s_mov_b32 s26, 0x20000
	s_mov_b32 s27, 0
	v_lshl_add_u64 v[198:199], v[198:199], 0, s[26:27]
	global_store_dwordx4 v[198:199], v[230:233], off nt
	s_nop 1
	s_waitcnt vmcnt(20)
	v_permlane16_swap_b32_e32 v4, v6
	v_permlane16_swap_b32_e32 v5, v7
	s_nop 1
	v_permlane32_swap_b32_e32 v4, v6
	v_permlane32_swap_b32_e32 v5, v7
	s_nop 1
	v_lshlrev_b32_e32 v226, 16, v4
	v_and_b32_e32 v227, 0xffff0000, v4
	v_lshlrev_b32_e32 v228, 16, v5
	v_and_b32_e32 v229, 0xffff0000, v5
	v_lshlrev_b32_e32 v230, 16, v6
	v_and_b32_e32 v231, 0xffff0000, v6
	v_lshlrev_b32_e32 v232, 16, v7
	v_and_b32_e32 v233, 0xffff0000, v7
	v_fma_f32 v226, v84, v184, v226
	v_fma_f32 v227, v85, v185, v227
	v_fma_f32 v228, v86, v186, v228
	v_fma_f32 v229, v87, v187, v229
	v_fma_f32 v230, v76, v188, v230
	v_fma_f32 v231, v77, v189, v231
	v_fma_f32 v232, v78, v190, v232
	v_fma_f32 v233, v79, v191, v233
	v_mov_b32_e32 v234, v230
	v_mov_b32_e32 v235, v231
	v_mov_b32_e32 v236, v232
	v_mov_b32_e32 v237, v233
	s_mov_b32 s26, 0x200000
	s_mov_b32 s27, 0
	v_lshl_add_u64 v[198:199], v[194:195], 0, s[26:27]
	v_mov_b32_dpp v230, v226 row_ror:8 row_mask:0xf bank_mask:0x3
	v_mov_b32_dpp v231, v227 row_ror:8 row_mask:0xf bank_mask:0x3
	v_mov_b32_dpp v232, v228 row_ror:8 row_mask:0xf bank_mask:0x3
	v_mov_b32_dpp v233, v229 row_ror:8 row_mask:0xf bank_mask:0x3
	v_mov_b32_dpp v226, v234 row_ror:8 row_mask:0xf bank_mask:0xc
	v_mov_b32_dpp v227, v235 row_ror:8 row_mask:0xf bank_mask:0xc
	v_mov_b32_dpp v228, v236 row_ror:8 row_mask:0xf bank_mask:0xc
	v_mov_b32_dpp v229, v237 row_ror:8 row_mask:0xf bank_mask:0xc
	global_store_dwordx4 v[198:199], v[226:229], off offset:512 nt
	s_mov_b32 s26, 0x20000
	s_mov_b32 s27, 0
	v_lshl_add_u64 v[198:199], v[198:199], 0, s[26:27]
	global_store_dwordx4 v[198:199], v[230:233], off offset:512 nt
	s_nop 1
	s_waitcnt vmcnt(19)
	v_permlane16_swap_b32_e32 v8, v10
	v_permlane16_swap_b32_e32 v9, v11
	s_nop 1
	v_permlane32_swap_b32_e32 v8, v10
	v_permlane32_swap_b32_e32 v9, v11
	s_nop 1
	v_lshlrev_b32_e32 v226, 16, v8
	v_and_b32_e32 v227, 0xffff0000, v8
	v_lshlrev_b32_e32 v228, 16, v9
	v_and_b32_e32 v229, 0xffff0000, v9
	v_lshlrev_b32_e32 v230, 16, v10
	v_and_b32_e32 v231, 0xffff0000, v10
	v_lshlrev_b32_e32 v232, 16, v11
	v_and_b32_e32 v233, 0xffff0000, v11
	v_fma_f32 v226, v80, v176, v226
	v_fma_f32 v227, v81, v177, v227
	v_fma_f32 v228, v82, v178, v228
	v_fma_f32 v229, v83, v179, v229
	v_fma_f32 v230, v72, v180, v230
	v_fma_f32 v231, v73, v181, v231
	v_fma_f32 v232, v74, v182, v232
	v_fma_f32 v233, v75, v183, v233
	v_mov_b32_e32 v234, v230
	v_mov_b32_e32 v235, v231
	v_mov_b32_e32 v236, v232
	v_mov_b32_e32 v237, v233
	s_mov_b32 s26, 0x240000
	s_mov_b32 s27, 0
	v_lshl_add_u64 v[198:199], v[194:195], 0, s[26:27]
	v_mov_b32_dpp v230, v226 row_ror:8 row_mask:0xf bank_mask:0x3
	v_mov_b32_dpp v231, v227 row_ror:8 row_mask:0xf bank_mask:0x3
	v_mov_b32_dpp v232, v228 row_ror:8 row_mask:0xf bank_mask:0x3
	v_mov_b32_dpp v233, v229 row_ror:8 row_mask:0xf bank_mask:0x3
	v_mov_b32_dpp v226, v234 row_ror:8 row_mask:0xf bank_mask:0xc
	v_mov_b32_dpp v227, v235 row_ror:8 row_mask:0xf bank_mask:0xc
	v_mov_b32_dpp v228, v236 row_ror:8 row_mask:0xf bank_mask:0xc
	v_mov_b32_dpp v229, v237 row_ror:8 row_mask:0xf bank_mask:0xc
	global_store_dwordx4 v[198:199], v[226:229], off nt
	s_mov_b32 s26, 0x20000
	s_mov_b32 s27, 0
	v_lshl_add_u64 v[198:199], v[198:199], 0, s[26:27]
	global_store_dwordx4 v[198:199], v[230:233], off nt
	s_nop 1
	s_waitcnt vmcnt(18)
	v_permlane16_swap_b32_e32 v12, v14
	v_permlane16_swap_b32_e32 v13, v15
	s_nop 1
	v_permlane32_swap_b32_e32 v12, v14
	v_permlane32_swap_b32_e32 v13, v15
	s_nop 1
	v_lshlrev_b32_e32 v226, 16, v12
	v_and_b32_e32 v227, 0xffff0000, v12
	v_lshlrev_b32_e32 v228, 16, v13
	v_and_b32_e32 v229, 0xffff0000, v13
	v_lshlrev_b32_e32 v230, 16, v14
	v_and_b32_e32 v231, 0xffff0000, v14
	v_lshlrev_b32_e32 v232, 16, v15
	v_and_b32_e32 v233, 0xffff0000, v15
	v_fma_f32 v226, v68, v184, v226
	v_fma_f32 v227, v69, v185, v227
	v_fma_f32 v228, v70, v186, v228
	v_fma_f32 v229, v71, v187, v229
	v_fma_f32 v230, v60, v188, v230
	v_fma_f32 v231, v61, v189, v231
	v_fma_f32 v232, v62, v190, v232
	v_fma_f32 v233, v63, v191, v233
	v_mov_b32_e32 v234, v230
	v_mov_b32_e32 v235, v231
	v_mov_b32_e32 v236, v232
	v_mov_b32_e32 v237, v233
	s_mov_b32 s26, 0x240000
	s_mov_b32 s27, 0
	v_lshl_add_u64 v[198:199], v[194:195], 0, s[26:27]
	v_mov_b32_dpp v230, v226 row_ror:8 row_mask:0xf bank_mask:0x3
	v_mov_b32_dpp v231, v227 row_ror:8 row_mask:0xf bank_mask:0x3
	v_mov_b32_dpp v232, v228 row_ror:8 row_mask:0xf bank_mask:0x3
	v_mov_b32_dpp v233, v229 row_ror:8 row_mask:0xf bank_mask:0x3
	v_mov_b32_dpp v226, v234 row_ror:8 row_mask:0xf bank_mask:0xc
	v_mov_b32_dpp v227, v235 row_ror:8 row_mask:0xf bank_mask:0xc
	v_mov_b32_dpp v228, v236 row_ror:8 row_mask:0xf bank_mask:0xc
	v_mov_b32_dpp v229, v237 row_ror:8 row_mask:0xf bank_mask:0xc
	global_store_dwordx4 v[198:199], v[226:229], off offset:512 nt
	s_mov_b32 s26, 0x20000
	s_mov_b32 s27, 0
	v_lshl_add_u64 v[198:199], v[198:199], 0, s[26:27]
	global_store_dwordx4 v[198:199], v[230:233], off offset:512 nt
	s_nop 1
	s_waitcnt vmcnt(17)
	v_permlane16_swap_b32_e32 v16, v18
	v_permlane16_swap_b32_e32 v17, v19
	s_nop 1
	v_permlane32_swap_b32_e32 v16, v18
	v_permlane32_swap_b32_e32 v17, v19
	s_nop 1
	v_lshlrev_b32_e32 v226, 16, v16
	v_and_b32_e32 v227, 0xffff0000, v16
	v_lshlrev_b32_e32 v228, 16, v17
	v_and_b32_e32 v229, 0xffff0000, v17
	v_lshlrev_b32_e32 v230, 16, v18
	v_and_b32_e32 v231, 0xffff0000, v18
	v_lshlrev_b32_e32 v232, 16, v19
	v_and_b32_e32 v233, 0xffff0000, v19
	v_fma_f32 v226, v64, v176, v226
	v_fma_f32 v227, v65, v177, v227
	v_fma_f32 v228, v66, v178, v228
	v_fma_f32 v229, v67, v179, v229
	v_fma_f32 v230, v56, v180, v230
	v_fma_f32 v231, v57, v181, v231
	v_fma_f32 v232, v58, v182, v232
	v_fma_f32 v233, v59, v183, v233
	v_mov_b32_e32 v234, v230
	v_mov_b32_e32 v235, v231
	v_mov_b32_e32 v236, v232
	v_mov_b32_e32 v237, v233
	s_mov_b32 s26, 0x280000
	s_mov_b32 s27, 0
	v_lshl_add_u64 v[198:199], v[194:195], 0, s[26:27]
	v_mov_b32_dpp v230, v226 row_ror:8 row_mask:0xf bank_mask:0x3
	v_mov_b32_dpp v231, v227 row_ror:8 row_mask:0xf bank_mask:0x3
	v_mov_b32_dpp v232, v228 row_ror:8 row_mask:0xf bank_mask:0x3
	v_mov_b32_dpp v233, v229 row_ror:8 row_mask:0xf bank_mask:0x3
	v_mov_b32_dpp v226, v234 row_ror:8 row_mask:0xf bank_mask:0xc
	v_mov_b32_dpp v227, v235 row_ror:8 row_mask:0xf bank_mask:0xc
	v_mov_b32_dpp v228, v236 row_ror:8 row_mask:0xf bank_mask:0xc
	v_mov_b32_dpp v229, v237 row_ror:8 row_mask:0xf bank_mask:0xc
	global_store_dwordx4 v[198:199], v[226:229], off nt
	s_mov_b32 s26, 0x20000
	s_mov_b32 s27, 0
	v_lshl_add_u64 v[198:199], v[198:199], 0, s[26:27]
	global_store_dwordx4 v[198:199], v[230:233], off nt
	s_nop 1
	s_waitcnt vmcnt(16)
	v_permlane16_swap_b32_e32 v20, v22
	v_permlane16_swap_b32_e32 v21, v23
	s_nop 1
	v_permlane32_swap_b32_e32 v20, v22
	v_permlane32_swap_b32_e32 v21, v23
	s_nop 1
	v_lshlrev_b32_e32 v226, 16, v20
	v_and_b32_e32 v227, 0xffff0000, v20
	v_lshlrev_b32_e32 v228, 16, v21
	v_and_b32_e32 v229, 0xffff0000, v21
	v_lshlrev_b32_e32 v230, 16, v22
	v_and_b32_e32 v231, 0xffff0000, v22
	v_lshlrev_b32_e32 v232, 16, v23
	v_and_b32_e32 v233, 0xffff0000, v23
	v_fma_f32 v226, v52, v184, v226
	v_fma_f32 v227, v53, v185, v227
	v_fma_f32 v228, v54, v186, v228
	v_fma_f32 v229, v55, v187, v229
	v_fma_f32 v230, v44, v188, v230
	v_fma_f32 v231, v45, v189, v231
	v_fma_f32 v232, v46, v190, v232
	v_fma_f32 v233, v47, v191, v233
	v_mov_b32_e32 v234, v230
	v_mov_b32_e32 v235, v231
	v_mov_b32_e32 v236, v232
	v_mov_b32_e32 v237, v233
	s_mov_b32 s26, 0x280000
	s_mov_b32 s27, 0
	v_lshl_add_u64 v[198:199], v[194:195], 0, s[26:27]
	v_mov_b32_dpp v230, v226 row_ror:8 row_mask:0xf bank_mask:0x3
	v_mov_b32_dpp v231, v227 row_ror:8 row_mask:0xf bank_mask:0x3
	v_mov_b32_dpp v232, v228 row_ror:8 row_mask:0xf bank_mask:0x3
	v_mov_b32_dpp v233, v229 row_ror:8 row_mask:0xf bank_mask:0x3
	v_mov_b32_dpp v226, v234 row_ror:8 row_mask:0xf bank_mask:0xc
	v_mov_b32_dpp v227, v235 row_ror:8 row_mask:0xf bank_mask:0xc
	v_mov_b32_dpp v228, v236 row_ror:8 row_mask:0xf bank_mask:0xc
	v_mov_b32_dpp v229, v237 row_ror:8 row_mask:0xf bank_mask:0xc
	global_store_dwordx4 v[198:199], v[226:229], off offset:512 nt
	s_mov_b32 s26, 0x20000
	s_mov_b32 s27, 0
	v_lshl_add_u64 v[198:199], v[198:199], 0, s[26:27]
	global_store_dwordx4 v[198:199], v[230:233], off offset:512 nt
	s_nop 1
	s_waitcnt vmcnt(15)
	v_permlane16_swap_b32_e32 v24, v26
	v_permlane16_swap_b32_e32 v25, v27
	s_nop 1
	v_permlane32_swap_b32_e32 v24, v26
	v_permlane32_swap_b32_e32 v25, v27
	s_nop 1
	v_lshlrev_b32_e32 v226, 16, v24
	v_and_b32_e32 v227, 0xffff0000, v24
	v_lshlrev_b32_e32 v228, 16, v25
	v_and_b32_e32 v229, 0xffff0000, v25
	v_lshlrev_b32_e32 v230, 16, v26
	v_and_b32_e32 v231, 0xffff0000, v26
	v_lshlrev_b32_e32 v232, 16, v27
	v_and_b32_e32 v233, 0xffff0000, v27
	v_fma_f32 v226, v48, v176, v226
	v_fma_f32 v227, v49, v177, v227
	v_fma_f32 v228, v50, v178, v228
	v_fma_f32 v229, v51, v179, v229
	v_fma_f32 v230, v40, v180, v230
	v_fma_f32 v231, v41, v181, v231
	v_fma_f32 v232, v42, v182, v232
	v_fma_f32 v233, v43, v183, v233
	v_mov_b32_e32 v234, v230
	v_mov_b32_e32 v235, v231
	v_mov_b32_e32 v236, v232
	v_mov_b32_e32 v237, v233
	s_mov_b32 s26, 0x2c0000
	s_mov_b32 s27, 0
	v_lshl_add_u64 v[198:199], v[194:195], 0, s[26:27]
	v_mov_b32_dpp v230, v226 row_ror:8 row_mask:0xf bank_mask:0x3
	v_mov_b32_dpp v231, v227 row_ror:8 row_mask:0xf bank_mask:0x3
	v_mov_b32_dpp v232, v228 row_ror:8 row_mask:0xf bank_mask:0x3
	v_mov_b32_dpp v233, v229 row_ror:8 row_mask:0xf bank_mask:0x3
	v_mov_b32_dpp v226, v234 row_ror:8 row_mask:0xf bank_mask:0xc
	v_mov_b32_dpp v227, v235 row_ror:8 row_mask:0xf bank_mask:0xc
	v_mov_b32_dpp v228, v236 row_ror:8 row_mask:0xf bank_mask:0xc
	v_mov_b32_dpp v229, v237 row_ror:8 row_mask:0xf bank_mask:0xc
	global_store_dwordx4 v[198:199], v[226:229], off nt
	s_mov_b32 s26, 0x20000
	s_mov_b32 s27, 0
	v_lshl_add_u64 v[198:199], v[198:199], 0, s[26:27]
	global_store_dwordx4 v[198:199], v[230:233], off nt
	s_nop 1
	s_waitcnt vmcnt(14)
	v_permlane16_swap_b32_e32 v28, v30
	v_permlane16_swap_b32_e32 v29, v31
	s_nop 1
	v_permlane32_swap_b32_e32 v28, v30
	v_permlane32_swap_b32_e32 v29, v31
	s_nop 1
	v_lshlrev_b32_e32 v226, 16, v28
	v_and_b32_e32 v227, 0xffff0000, v28
	v_lshlrev_b32_e32 v228, 16, v29
	v_and_b32_e32 v229, 0xffff0000, v29
	v_lshlrev_b32_e32 v230, 16, v30
	v_and_b32_e32 v231, 0xffff0000, v30
	v_lshlrev_b32_e32 v232, 16, v31
	v_and_b32_e32 v233, 0xffff0000, v31
	v_fma_f32 v226, v36, v184, v226
	v_fma_f32 v227, v37, v185, v227
	v_fma_f32 v228, v38, v186, v228
	v_fma_f32 v229, v39, v187, v229
	v_fma_f32 v230, v32, v188, v230
	v_fma_f32 v231, v33, v189, v231
	v_fma_f32 v232, v34, v190, v232
	v_fma_f32 v233, v35, v191, v233
	v_mov_b32_e32 v234, v230
	v_mov_b32_e32 v235, v231
	v_mov_b32_e32 v236, v232
	v_mov_b32_e32 v237, v233
	s_mov_b32 s26, 0x2c0000
	s_mov_b32 s27, 0
	v_lshl_add_u64 v[198:199], v[194:195], 0, s[26:27]
	v_mov_b32_dpp v230, v226 row_ror:8 row_mask:0xf bank_mask:0x3
	v_mov_b32_dpp v231, v227 row_ror:8 row_mask:0xf bank_mask:0x3
	v_mov_b32_dpp v232, v228 row_ror:8 row_mask:0xf bank_mask:0x3
	v_mov_b32_dpp v233, v229 row_ror:8 row_mask:0xf bank_mask:0x3
	v_mov_b32_dpp v226, v234 row_ror:8 row_mask:0xf bank_mask:0xc
	v_mov_b32_dpp v227, v235 row_ror:8 row_mask:0xf bank_mask:0xc
	v_mov_b32_dpp v228, v236 row_ror:8 row_mask:0xf bank_mask:0xc
	v_mov_b32_dpp v229, v237 row_ror:8 row_mask:0xf bank_mask:0xc
	global_store_dwordx4 v[198:199], v[226:229], off offset:512 nt
	s_mov_b32 s26, 0x20000
	s_mov_b32 s27, 0
	v_lshl_add_u64 v[198:199], v[198:199], 0, s[26:27]
	global_store_dwordx4 v[198:199], v[230:233], off offset:512 nt
	s_nop 1
	s_cbranch_vccnz .LBB0_1350
	s_andn2_b64 vcc, exec, s[6:7]
	s_cbranch_vccnz .LBB0_1349
	s_barrier
	s_branch .LBB0_1349
